# baseline (speedup 1.0000x reference)
.LBB0_28:
	v_mov_b32_e32 v41, v236
	v_mov_b32_e32 v32, v236
	v_and_b32_e32 v40, 15, v215
	s_nop 0
	v_permlane16_swap_b32_e32 v41, v32
	s_nop 0
	v_add_f32_e32 v41, v41, v32
	v_mov_b32_e32 v32, v41
	v_cmp_gt_u32_e32 vcc, 5, v40
	s_nop 0
	v_permlane32_swap_b32_e32 v41, v32
	s_nop 0
	s_and_saveexec_b64 s[0:1], vcc
	s_cbranch_execz .LBB0_21
	s_waitcnt lgkmcnt(0)
	v_add_f32_e32 v32, v41, v32
	v_div_scale_f32 v33, s[10:11], v32, v32, 0.5
	v_rcp_f32_e32 v34, v33
	v_div_scale_f32 v35, vcc, 0.5, v32, 0.5
	v_fma_f32 v36, -v33, v34, 1.0
	v_fmac_f32_e32 v34, v36, v34
	v_mul_f32_e32 v36, v35, v34
	v_fma_f32 v37, -v33, v36, v35
	v_fmac_f32_e32 v36, v37, v34
	v_fma_f32 v33, -v33, v36, v35
	v_div_fmas_f32 v33, v33, v34, v36
	v_div_fixup_f32 v32, v33, v32, 0.5
	v_add_u32_e32 v33, s3, v221
	v_mov_b32_e32 v34, v40
	v_mad_u64_u32 v[34:35], s[8:9], v33, 5, v[34:35]
	v_sub_u32_e32 v36, v222, v214
	v_lshrrev_b32_e32 v37, 4, v215
	v_lshl_add_u32 v36, v37, 3, v36
	v_lshl_add_u32 v33, v34, 7, v36
	v_pk_mul_f32 v[44:45], v[32:33], v[0:1] op_sel_hi:[0,1]
	v_pk_mul_f32 v[46:47], v[32:33], v[2:3] op_sel_hi:[0,1]
	v_cvt_pk_f16_f32 v44, v44, v45
	v_cvt_pk_f16_f32 v45, v46, v47
	ds_write_b64 v33, v[44:45]
	v_pk_mul_f32 v[48:49], v[32:33], v[4:5] op_sel_hi:[0,1]
	v_pk_mul_f32 v[50:51], v[32:33], v[6:7] op_sel_hi:[0,1]
	v_cvt_pk_f16_f32 v48, v48, v49
	v_cvt_pk_f16_f32 v49, v50, v51
	ds_write_b64 v33, v[48:49] offset:32
	v_pk_mul_f32 v[52:53], v[32:33], v[8:9] op_sel_hi:[0,1]
	v_pk_mul_f32 v[54:55], v[32:33], v[10:11] op_sel_hi:[0,1]
	v_cvt_pk_f16_f32 v52, v52, v53
	v_cvt_pk_f16_f32 v53, v54, v55
	ds_write_b64 v33, v[52:53] offset:64
	v_pk_mul_f32 v[56:57], v[32:33], v[12:13] op_sel_hi:[0,1]
	v_pk_mul_f32 v[58:59], v[32:33], v[14:15] op_sel_hi:[0,1]
	v_cvt_pk_f16_f32 v56, v56, v57
	v_cvt_pk_f16_f32 v57, v58, v59
	ds_write_b64 v33, v[56:57] offset:96
	s_branch .LBB0_21
